# in-lane threshold-bin scan: 8 readlanes + 4-op scalar scan per bin (on top of v62)
# baseline (speedup 1.0000x reference)
.Lthr_found:
	v_readlane_b32 s25, v9, s0
	v_readlane_b32 s26, v8, s0
	v_readlane_b32 s27, v7, s0
	v_readlane_b32 s28, v6, s0
	v_readlane_b32 s29, v5, s0
	v_readlane_b32 s30, v4, s0
	v_readlane_b32 s31, v3, s0
	v_readlane_b32 s34, v2, s0
	s_add_i32 s1, s8, s25
	s_cmpk_gt_u32 s1, 0xff
	s_cbranch_scc1 .Lthr_b7
	s_mov_b32 s8, s1
	s_add_i32 s1, s8, s26
	s_cmpk_gt_u32 s1, 0xff
	s_cbranch_scc1 .Lthr_b6
	s_mov_b32 s8, s1
	s_add_i32 s1, s8, s27
	s_cmpk_gt_u32 s1, 0xff
	s_cbranch_scc1 .Lthr_b5
	s_mov_b32 s8, s1
	s_add_i32 s1, s8, s28
	s_cmpk_gt_u32 s1, 0xff
	s_cbranch_scc1 .Lthr_b4
	s_mov_b32 s8, s1
	s_add_i32 s1, s8, s29
	s_cmpk_gt_u32 s1, 0xff
	s_cbranch_scc1 .Lthr_b3
	s_mov_b32 s8, s1
	s_add_i32 s1, s8, s30
	s_cmpk_gt_u32 s1, 0xff
	s_cbranch_scc1 .Lthr_b2
	s_mov_b32 s8, s1
	s_add_i32 s1, s8, s31
	s_cmpk_gt_u32 s1, 0xff
	s_cbranch_scc1 .Lthr_b1
	s_mov_b32 s8, s1
	s_mov_b32 s94, 0
	s_branch .Lthr_bjoin
.Lthr_b7:
	s_mov_b32 s94, 7
	s_branch .Lthr_bjoin
.Lthr_b6:
	s_mov_b32 s94, 6
	s_branch .Lthr_bjoin
.Lthr_b5:
	s_mov_b32 s94, 5
	s_branch .Lthr_bjoin
.Lthr_b4:
	s_mov_b32 s94, 4
	s_branch .Lthr_bjoin
.Lthr_b3:
	s_mov_b32 s94, 3
	s_branch .Lthr_bjoin
.Lthr_b2:
	s_mov_b32 s94, 2
	s_branch .Lthr_bjoin
.Lthr_b1:
	s_mov_b32 s94, 1
.Lthr_bjoin:
	s_lshl_b32 s0, s0, 3
	s_add_i32 s94, s94, s0
	v_readlane_b32 s0, v254, 54
	s_lshl_b32 s22, s94, 7
	v_mov_b32_e32 v91, 0
	v_mov_b32_e32 v7, 0xffff0000
	v_lshl_add_u32 v79, v10, 2, s0
	s_and_b64 vcc, exec, s[60:61]
	s_cbranch_vccz .LBB0_726
	v_cmp_ge_u32_sdwa vcc, v77, s22 src0_sel:WORD_0 src1_sel:DWORD
	s_mov_b32 s0, 0xffff
	v_lshl_or_b32 v2, v77, 16, s0
	v_lshl_add_u32 v5, v91, 8, v79
	ds_write_b32 v5, v2
	v_addc_co_u32_e32 v91, vcc, 0, v91, vcc
	v_cmp_ge_u32_sdwa vcc, v77, s22 src0_sel:WORD_1 src1_sel:DWORD
	s_mov_b32 s1, 0xfffe
	v_and_or_b32 v3, v77, v7, s1
	v_lshl_add_u32 v6, v91, 8, v79
	ds_write_b32 v6, v3
	v_addc_co_u32_e32 v91, vcc, 0, v91, vcc
	v_cmp_ge_u32_sdwa vcc, v76, s22 src0_sel:WORD_0 src1_sel:DWORD
	s_mov_b32 s0, 0xff7f
	v_lshl_or_b32 v4, v76, 16, s0
	v_lshl_add_u32 v5, v91, 8, v79
	ds_write_b32 v5, v4
	v_addc_co_u32_e32 v91, vcc, 0, v91, vcc
	v_cmp_ge_u32_sdwa vcc, v76, s22 src0_sel:WORD_1 src1_sel:DWORD
	s_mov_b32 s1, 0xff7e
	v_and_or_b32 v2, v76, v7, s1
	v_lshl_add_u32 v6, v91, 8, v79
	ds_write_b32 v6, v2
	v_addc_co_u32_e32 v91, vcc, 0, v91, vcc
	v_cmp_ge_u32_sdwa vcc, v75, s22 src0_sel:WORD_0 src1_sel:DWORD
	s_mov_b32 s0, 0xfeff
	v_lshl_or_b32 v3, v75, 16, s0
	v_lshl_add_u32 v5, v91, 8, v79
	ds_write_b32 v5, v3
	v_addc_co_u32_e32 v91, vcc, 0, v91, vcc
	v_cmp_ge_u32_sdwa vcc, v75, s22 src0_sel:WORD_1 src1_sel:DWORD
	s_mov_b32 s1, 0xfefe
	v_and_or_b32 v4, v75, v7, s1
	v_lshl_add_u32 v6, v91, 8, v79
	ds_write_b32 v6, v4
	v_addc_co_u32_e32 v91, vcc, 0, v91, vcc
	v_cmp_ge_u32_sdwa vcc, v74, s22 src0_sel:WORD_0 src1_sel:DWORD
	s_mov_b32 s0, 0xfe7f
	v_lshl_or_b32 v2, v74, 16, s0
	v_lshl_add_u32 v5, v91, 8, v79
	ds_write_b32 v5, v2
	v_addc_co_u32_e32 v91, vcc, 0, v91, vcc
	v_cmp_ge_u32_sdwa vcc, v74, s22 src0_sel:WORD_1 src1_sel:DWORD
	s_mov_b32 s1, 0xfe7e
	v_and_or_b32 v3, v74, v7, s1
	v_lshl_add_u32 v6, v91, 8, v79
	ds_write_b32 v6, v3
	v_addc_co_u32_e32 v91, vcc, 0, v91, vcc
	v_min_u32_e32 v91, 21, v91
	v_cmp_ge_u32_sdwa vcc, v73, s22 src0_sel:WORD_0 src1_sel:DWORD
	s_mov_b32 s0, 0xfdff
	v_lshl_or_b32 v4, v73, 16, s0
	v_lshl_add_u32 v5, v91, 8, v79
	ds_write_b32 v5, v4
	v_addc_co_u32_e32 v91, vcc, 0, v91, vcc
	v_cmp_ge_u32_sdwa vcc, v73, s22 src0_sel:WORD_1 src1_sel:DWORD
	s_mov_b32 s1, 0xfdfe
	v_and_or_b32 v2, v73, v7, s1
	v_lshl_add_u32 v6, v91, 8, v79
	ds_write_b32 v6, v2
	v_addc_co_u32_e32 v91, vcc, 0, v91, vcc
	v_cmp_ge_u32_sdwa vcc, v72, s22 src0_sel:WORD_0 src1_sel:DWORD
	s_mov_b32 s0, 0xfd7f
	v_lshl_or_b32 v3, v72, 16, s0
	v_lshl_add_u32 v5, v91, 8, v79
	ds_write_b32 v5, v3
	v_addc_co_u32_e32 v91, vcc, 0, v91, vcc
	v_cmp_ge_u32_sdwa vcc, v72, s22 src0_sel:WORD_1 src1_sel:DWORD
	s_mov_b32 s1, 0xfd7e
	v_and_or_b32 v4, v72, v7, s1
	v_lshl_add_u32 v6, v91, 8, v79
	ds_write_b32 v6, v4
	v_addc_co_u32_e32 v91, vcc, 0, v91, vcc
	v_cmp_ge_u32_sdwa vcc, v71, s22 src0_sel:WORD_0 src1_sel:DWORD
	s_mov_b32 s0, 0xfcff
	v_lshl_or_b32 v2, v71, 16, s0
	v_lshl_add_u32 v5, v91, 8, v79
	ds_write_b32 v5, v2
	v_addc_co_u32_e32 v91, vcc, 0, v91, vcc
	v_cmp_ge_u32_sdwa vcc, v71, s22 src0_sel:WORD_1 src1_sel:DWORD
	s_mov_b32 s1, 0xfcfe
	v_and_or_b32 v3, v71, v7, s1
	v_lshl_add_u32 v6, v91, 8, v79
	ds_write_b32 v6, v3
	v_addc_co_u32_e32 v91, vcc, 0, v91, vcc
	v_cmp_ge_u32_sdwa vcc, v70, s22 src0_sel:WORD_0 src1_sel:DWORD
	s_mov_b32 s0, 0xfc7f
	v_lshl_or_b32 v4, v70, 16, s0
	v_lshl_add_u32 v5, v91, 8, v79
	ds_write_b32 v5, v4
	v_addc_co_u32_e32 v91, vcc, 0, v91, vcc
	v_cmp_ge_u32_sdwa vcc, v70, s22 src0_sel:WORD_1 src1_sel:DWORD
	s_mov_b32 s1, 0xfc7e
	v_and_or_b32 v2, v70, v7, s1
	v_lshl_add_u32 v6, v91, 8, v79
	ds_write_b32 v6, v2
	v_addc_co_u32_e32 v91, vcc, 0, v91, vcc
	v_min_u32_e32 v91, 21, v91
